# GEMM K-loops: every MFMA run on an 8-byte boundary (one s_nop before and after the second compute segment) plus 64-byte loop heads, on top of combo5
# baseline (speedup 1.0000x reference)
; #define PG8_STAGE(bufoff, gbase, voff) do { _Pragma("unroll") for (int _i = 0; _i < 2; ++_i) \
;         __builtin_amdgcn_global_load_lds((const unsigned*)((const char*)(gbase) + (voff)[_i]), (PG8_LAS unsigned*)(lds + (bufoff) + ldsw + _i * 8192), 16, 0, 0); } while (0)
; #define PG8_LDA(dst, b, h) do { _Pragma("unroll") for (int m = 0; m < 4; ++m) _Pragma("unroll") for (int k = 0; k < 2; ++k) dst[m][k] = *(const PG8_LAS bf16x8*)(lds + PG8_SA(b, h) + aoff + m * 2048 + k * 1024); } while (0)
; #define PG8_LDB(dst, b, h) do { _Pragma("unroll") for (int n = 0; n < 2; ++n) _Pragma("unroll") for (int k = 0; k < 2; ++k) dst[n][k] = *(const PG8_LAS bf16x8*)(lds + PG8_SB(b, h) + boff + n * 2048 + k * 1024); } while (0)
; #define PG8_MMA(ai, bj, At, Bt) do { __builtin_amdgcn_s_setprio(1); _Pragma("unroll") for (int m = 0; m < 4; ++m) _Pragma("unroll") for (int n = 0; n < 2; ++n) _Pragma("unroll") for (int k = 0; k < 2; ++k) \
;         acc[ai][bj][m][n] = __builtin_amdgcn_mfma_f32_16x16x32_bf16(Bt[n][k], At[m][k], acc[ai][bj][m][n], 0, 0, 0); __builtin_amdgcn_s_setprio(0); } while (0)
; #define PG8_WAIT_V(n) asm volatile("s_waitcnt vmcnt(" #n ")" ::: "memory")
; #define PG8_WAIT_L(n) asm volatile("s_waitcnt lgkmcnt(" #n ")" ::: "memory")
; #define PG8_BAR __builtin_amdgcn_s_barrier()
; #define PG8_SCHED __builtin_amdgcn_sched_barrier(0)
; template <class Epi, class Sched, bool ALIGN_EPI = false, bool SP2 = false>
; __device__ __forceinline__ void gemm_phase(PG8_LAS unsigned char* lds, const Gemm g, const Sched& S, const Epi& E) {
;     ...
;             PG8_LDB(B0, 0, 0); PG8_LDB(B1, 0, 1); PG8_SCHED; PG8_LDA(At, 0, 0); PG8_STAGE(PG8_SA(1, 1), a1 + hstep, voffA);
;             PG8_WAIT_V(8); PG8_WAIT_L(0); PG8_BAR; PG8_MMA(0, 0, At, B0); PG8_MMA(0, 1, At, B1); PG8_BAR; PG8_SCHED;
;             PG8_LDA(At, 0, 1); PG8_STAGE(PG8_SB(0, 0), b2, voffB); PG8_STAGE(PG8_SB(0, 1), b2 + hstep, voffB); PG8_STAGE(PG8_SA(0, 0), a2, voffA);
;             PG8_WAIT_V(8); PG8_WAIT_L(0); PG8_BAR; PG8_MMA(1, 0, At, B0); PG8_MMA(1, 1, At, B1); PG8_BAR; PG8_SCHED;
.LBB0_102:
	ds_read_b128 v[154:157], v159
	ds_read_b128 v[162:165], v159 offset:1024
	ds_read_b128 v[166:169], v159 offset:2048
	ds_read_b128 v[170:173], v159 offset:3072
	ds_read_b128 v[174:177], v160
	ds_read_b128 v[178:181], v160 offset:1024
	ds_read_b128 v[184:187], v160 offset:2048
	ds_read_b128 v[188:191], v160 offset:3072
	s_add_u32 s26, s24, 0xfff00080
	s_addc_u32 s27, s25, -1
	s_cmp_eq_u32 s50, 60
	s_cselect_b32 s29, s17, s27
	s_cselect_b32 s28, s23, s26
	s_cselect_b32 s27, s15, s49
	s_cselect_b32 s26, s46, s47
	v_lshl_add_u64 v[224:225], s[24:25], 0, v[146:147]
	s_add_i32 m0, s34, 0xc000
	ds_read_b128 v[192:195], v161
	ds_read_b128 v[196:199], v161 offset:1024
	ds_read_b128 v[200:203], v161 offset:2048
	ds_read_b128 v[204:207], v161 offset:3072
	ds_read_b128 v[208:211], v161 offset:4096
	ds_read_b128 v[212:215], v161 offset:5120
	ds_read_b128 v[216:219], v161 offset:6144
	ds_read_b128 v[220:223], v161 offset:7168
	global_load_lds_dwordx4 v[224:225], off
	v_lshl_add_u64 v[224:225], s[24:25], 0, v[148:149]
	s_add_i32 m0, s34, 0xe000
	s_nop 0
	global_load_lds_dwordx4 v[224:225], off
	s_waitcnt vmcnt(8)
	s_waitcnt lgkmcnt(0)
	s_barrier
	s_setprio 1
	s_waitcnt lgkmcnt(0)
	v_mfma_f32_16x16x32_bf16 v[126:129], v[154:157], v[192:195], v[126:129]
	v_mfma_f32_16x16x32_bf16 v[122:125], v[166:169], v[192:195], v[122:125]
	v_mfma_f32_16x16x32_bf16 v[110:113], v[154:157], v[200:203], v[110:113]
	v_mfma_f32_16x16x32_bf16 v[106:109], v[166:169], v[200:203], v[106:109]
	v_mfma_f32_16x16x32_bf16 v[98:101], v[154:157], v[208:211], v[98:101]
	v_mfma_f32_16x16x32_bf16 v[90:93], v[166:169], v[208:211], v[90:93]
	v_mfma_f32_16x16x32_bf16 v[82:85], v[154:157], v[216:219], v[82:85]
	v_mfma_f32_16x16x32_bf16 v[74:77], v[166:169], v[216:219], v[74:77]
	v_mfma_f32_16x16x32_bf16 v[126:129], v[162:165], v[196:199], v[126:129]
	v_mfma_f32_16x16x32_bf16 v[122:125], v[170:173], v[196:199], v[122:125]
	v_mfma_f32_16x16x32_bf16 v[110:113], v[162:165], v[204:207], v[110:113]
	v_mfma_f32_16x16x32_bf16 v[106:109], v[170:173], v[204:207], v[106:109]
	v_mfma_f32_16x16x32_bf16 v[98:101], v[162:165], v[212:215], v[98:101]
	v_mfma_f32_16x16x32_bf16 v[90:93], v[170:173], v[212:215], v[90:93]
	v_mfma_f32_16x16x32_bf16 v[82:85], v[162:165], v[220:223], v[82:85]
	v_mfma_f32_16x16x32_bf16 v[74:77], v[170:173], v[220:223], v[74:77]
	s_setprio 0
	s_setprio 1
	v_mfma_f32_16x16x32_bf16 v[118:121], v[174:177], v[192:195], v[118:121]
	v_mfma_f32_16x16x32_bf16 v[114:117], v[184:187], v[192:195], v[114:117]
	v_mfma_f32_16x16x32_bf16 v[102:105], v[174:177], v[200:203], v[102:105]
	v_mfma_f32_16x16x32_bf16 v[94:97], v[184:187], v[200:203], v[94:97]
	v_mfma_f32_16x16x32_bf16 v[86:89], v[174:177], v[208:211], v[86:89]
	v_mfma_f32_16x16x32_bf16 v[78:81], v[184:187], v[208:211], v[78:81]
	v_mfma_f32_16x16x32_bf16 v[70:73], v[174:177], v[216:219], v[70:73]
	v_mfma_f32_16x16x32_bf16 v[66:69], v[184:187], v[216:219], v[66:69]
	v_mfma_f32_16x16x32_bf16 v[118:121], v[178:181], v[196:199], v[118:121]
	v_mfma_f32_16x16x32_bf16 v[114:117], v[188:191], v[196:199], v[114:117]
	v_mfma_f32_16x16x32_bf16 v[102:105], v[178:181], v[204:207], v[102:105]
	v_mfma_f32_16x16x32_bf16 v[94:97], v[188:191], v[204:207], v[94:97]
	v_mfma_f32_16x16x32_bf16 v[86:89], v[178:181], v[212:215], v[86:89]
	v_mfma_f32_16x16x32_bf16 v[78:81], v[188:191], v[212:215], v[78:81]
	v_mfma_f32_16x16x32_bf16 v[70:73], v[178:181], v[220:223], v[70:73]
	v_mfma_f32_16x16x32_bf16 v[66:69], v[188:191], v[220:223], v[66:69]
	s_setprio 0
	s_barrier
	s_nop 0
	s_add_i32 s51, s42, s30
	v_lshl_add_u64 v[224:225], s[26:27], 0, v[140:141]
	s_mov_b32 m0, s51
	ds_read_b128 v[192:195], v161 offset:16384
	ds_read_b128 v[196:199], v161 offset:17408
	ds_read_b128 v[200:203], v161 offset:18432
	ds_read_b128 v[204:207], v161 offset:19456
	ds_read_b128 v[208:211], v161 offset:20480
	ds_read_b128 v[212:215], v161 offset:21504
	ds_read_b128 v[216:219], v161 offset:22528
	ds_read_b128 v[220:223], v161 offset:23552
	global_load_lds_dwordx4 v[224:225], off
	s_add_i32 m0, s51, 0x2000
	s_add_u32 s52, s26, 0x100000
	v_lshl_add_u64 v[226:227], s[26:27], 0, v[136:137]
	s_addc_u32 s53, s27, 0
	s_add_i32 s51, s43, s30
	global_load_lds_dwordx4 v[226:227], off
	v_lshl_add_u64 v[228:229], s[52:53], 0, v[140:141]
	s_mov_b32 m0, s51
	v_lshl_add_u64 v[230:231], s[28:29], 0, v[138:139]
	global_load_lds_dwordx4 v[228:229], off
	v_lshl_add_u64 v[228:229], s[52:53], 0, v[136:137]
	s_add_i32 m0, s51, 0x2000
	s_nop 0
	global_load_lds_dwordx4 v[228:229], off
	v_lshl_add_u64 v[228:229], s[28:29], 0, v[142:143]
	s_mov_b32 m0, s34
	s_nop 0
	global_load_lds_dwordx4 v[228:229], off
	s_mov_b32 m0, s35
	s_nop 0
	global_load_lds_dwordx4 v[230:231], off
	s_waitcnt vmcnt(8)
	s_waitcnt lgkmcnt(0)
	s_barrier
; #define PG8_STAGE(bufoff, gbase, voff) do { _Pragma("unroll") for (int _i = 0; _i < 2; ++_i) \
;         __builtin_amdgcn_global_load_lds((const unsigned*)((const char*)(gbase) + (voff)[_i]), (PG8_LAS unsigned*)(lds + (bufoff) + ldsw + _i * 8192), 16, 0, 0); } while (0)
; #define PG8_LDA(dst, b, h) do { _Pragma("unroll") for (int m = 0; m < 4; ++m) _Pragma("unroll") for (int k = 0; k < 2; ++k) dst[m][k] = *(const PG8_LAS bf16x8*)(lds + PG8_SA(b, h) + aoff + m * 2048 + k * 1024); } while (0)
; #define PG8_LDB(dst, b, h) do { _Pragma("unroll") for (int n = 0; n < 2; ++n) _Pragma("unroll") for (int k = 0; k < 2; ++k) dst[n][k] = *(const PG8_LAS bf16x8*)(lds + PG8_SB(b, h) + boff + n * 2048 + k * 1024); } while (0)
; #define PG8_MMA(ai, bj, At, Bt) do { __builtin_amdgcn_s_setprio(1); _Pragma("unroll") for (int m = 0; m < 4; ++m) _Pragma("unroll") for (int n = 0; n < 2; ++n) _Pragma("unroll") for (int k = 0; k < 2; ++k) \
;         acc[ai][bj][m][n] = __builtin_amdgcn_mfma_f32_16x16x32_bf16(Bt[n][k], At[m][k], acc[ai][bj][m][n], 0, 0, 0); __builtin_amdgcn_s_setprio(0); } while (0)
; #define PG8_WAIT_V(n) asm volatile("s_waitcnt vmcnt(" #n ")" ::: "memory")
; #define PG8_WAIT_L(n) asm volatile("s_waitcnt lgkmcnt(" #n ")" ::: "memory")
; #define PG8_BAR __builtin_amdgcn_s_barrier()
; #define PG8_SCHED __builtin_amdgcn_sched_barrier(0)
; template <class Epi, class Sched, bool ALIGN_EPI = false, bool SP2 = false>
; __device__ __forceinline__ void gemm_phase(PG8_LAS unsigned char* lds, const Gemm g, const Sched& S, const Epi& E) {
;     ...
;             PG8_WAIT_V(8); PG8_WAIT_L(0); PG8_BAR; PG8_MMA(1, 0, At, B0); PG8_MMA(1, 1, At, B1); PG8_BAR; PG8_SCHED;
;             PG8_LDB(B0, 1, 0); PG8_LDB(B1, 1, 1); PG8_SCHED; PG8_LDA(At, 1, 0); PG8_STAGE(PG8_SA(0, 1), a2 + hstep, voffA);
;             PG8_WAIT_V(8); PG8_WAIT_L(0); PG8_BAR; PG8_MMA(0, 0, At, B0); PG8_MMA(0, 1, At, B1); PG8_BAR; PG8_SCHED;
	s_setprio 1
	s_waitcnt lgkmcnt(0)
	v_mfma_f32_16x16x32_bf16 v[62:65], v[154:157], v[192:195], v[62:65]
	v_mfma_f32_16x16x32_bf16 v[58:61], v[166:169], v[192:195], v[58:61]
	v_mfma_f32_16x16x32_bf16 v[50:53], v[154:157], v[200:203], v[50:53]
	v_mfma_f32_16x16x32_bf16 v[42:45], v[166:169], v[200:203], v[42:45]
	v_mfma_f32_16x16x32_bf16 v[34:37], v[154:157], v[208:211], v[34:37]
	v_mfma_f32_16x16x32_bf16 v[26:29], v[166:169], v[208:211], v[26:29]
	v_mfma_f32_16x16x32_bf16 v[18:21], v[154:157], v[216:219], v[18:21]
	v_mfma_f32_16x16x32_bf16 v[10:13], v[166:169], v[216:219], v[10:13]
	v_mfma_f32_16x16x32_bf16 v[62:65], v[162:165], v[196:199], v[62:65]
	v_mfma_f32_16x16x32_bf16 v[58:61], v[170:173], v[196:199], v[58:61]
	v_mfma_f32_16x16x32_bf16 v[50:53], v[162:165], v[204:207], v[50:53]
	v_mfma_f32_16x16x32_bf16 v[42:45], v[170:173], v[204:207], v[42:45]
	v_mfma_f32_16x16x32_bf16 v[34:37], v[162:165], v[212:215], v[34:37]
	v_mfma_f32_16x16x32_bf16 v[26:29], v[170:173], v[212:215], v[26:29]
	v_mfma_f32_16x16x32_bf16 v[18:21], v[162:165], v[220:223], v[18:21]
	v_mfma_f32_16x16x32_bf16 v[10:13], v[170:173], v[220:223], v[10:13]
	s_setprio 0
	s_setprio 1
	v_mfma_f32_16x16x32_bf16 v[54:57], v[174:177], v[192:195], v[54:57]
	v_mfma_f32_16x16x32_bf16 v[46:49], v[184:187], v[192:195], v[46:49]
	v_mfma_f32_16x16x32_bf16 v[38:41], v[174:177], v[200:203], v[38:41]
	v_mfma_f32_16x16x32_bf16 v[30:33], v[184:187], v[200:203], v[30:33]
	v_mfma_f32_16x16x32_bf16 v[22:25], v[174:177], v[208:211], v[22:25]
	v_mfma_f32_16x16x32_bf16 v[14:17], v[184:187], v[208:211], v[14:17]
	v_mfma_f32_16x16x32_bf16 v[6:9], v[174:177], v[216:219], v[6:9]
	v_mfma_f32_16x16x32_bf16 v[2:5], v[184:187], v[216:219], v[2:5]
	v_mfma_f32_16x16x32_bf16 v[54:57], v[178:181], v[196:199], v[54:57]
	v_mfma_f32_16x16x32_bf16 v[46:49], v[188:191], v[196:199], v[46:49]
	v_mfma_f32_16x16x32_bf16 v[38:41], v[178:181], v[204:207], v[38:41]
	v_mfma_f32_16x16x32_bf16 v[30:33], v[188:191], v[204:207], v[30:33]
	v_mfma_f32_16x16x32_bf16 v[22:25], v[178:181], v[212:215], v[22:25]
	v_mfma_f32_16x16x32_bf16 v[14:17], v[188:191], v[212:215], v[14:17]
	v_mfma_f32_16x16x32_bf16 v[6:9], v[178:181], v[220:223], v[6:9]
	v_mfma_f32_16x16x32_bf16 v[2:5], v[188:191], v[220:223], v[2:5]
	s_setprio 0
	s_barrier
	s_nop 0
	s_add_i32 s51, 0, 0x18000
	v_add_u32_e32 v144, s51, v133
	s_add_i32 s52, 0, 0x1c000
	ds_read_b128 v[154:157], v144
	ds_read_b128 v[162:165], v144 offset:1024
	ds_read_b128 v[166:169], v144 offset:2048
	ds_read_b128 v[170:173], v144 offset:3072
	v_add_u32_e32 v144, s52, v133
	ds_read_b128 v[174:177], v144
	ds_read_b128 v[178:181], v144 offset:1024
	ds_read_b128 v[184:187], v144 offset:2048
	ds_read_b128 v[188:191], v144 offset:3072
	s_add_u32 s28, s28, 0x100000
	s_addc_u32 s29, s29, 0
	s_mov_b32 m0, s36
	v_lshl_add_u64 v[232:233], s[28:29], 0, v[142:143]
	ds_read_b128 v[192:195], v161 offset:32768
	ds_read_b128 v[196:199], v161 offset:33792
	ds_read_b128 v[200:203], v161 offset:34816
	ds_read_b128 v[204:207], v161 offset:35840
	ds_read_b128 v[208:211], v161 offset:36864
	ds_read_b128 v[212:215], v161 offset:37888
	ds_read_b128 v[216:219], v161 offset:38912
	ds_read_b128 v[220:223], v161 offset:39936
	global_load_lds_dwordx4 v[232:233], off
	v_lshl_add_u64 v[232:233], s[28:29], 0, v[138:139]
	s_mov_b32 m0, s37
	s_nop 0
	global_load_lds_dwordx4 v[232:233], off
	s_waitcnt vmcnt(8)
	s_waitcnt lgkmcnt(0)
	s_barrier
	s_setprio 1
	s_waitcnt lgkmcnt(0)
	v_mfma_f32_16x16x32_bf16 v[126:129], v[154:157], v[192:195], v[126:129]
	v_mfma_f32_16x16x32_bf16 v[122:125], v[166:169], v[192:195], v[122:125]
	v_mfma_f32_16x16x32_bf16 v[110:113], v[154:157], v[200:203], v[110:113]
	v_mfma_f32_16x16x32_bf16 v[106:109], v[166:169], v[200:203], v[106:109]
	v_mfma_f32_16x16x32_bf16 v[98:101], v[154:157], v[208:211], v[98:101]
	v_mfma_f32_16x16x32_bf16 v[90:93], v[166:169], v[208:211], v[90:93]
	v_mfma_f32_16x16x32_bf16 v[82:85], v[154:157], v[216:219], v[82:85]
	v_mfma_f32_16x16x32_bf16 v[74:77], v[166:169], v[216:219], v[74:77]
	v_mfma_f32_16x16x32_bf16 v[126:129], v[162:165], v[196:199], v[126:129]
	v_mfma_f32_16x16x32_bf16 v[122:125], v[170:173], v[196:199], v[122:125]
	v_mfma_f32_16x16x32_bf16 v[110:113], v[162:165], v[204:207], v[110:113]
	v_mfma_f32_16x16x32_bf16 v[106:109], v[170:173], v[204:207], v[106:109]
	v_mfma_f32_16x16x32_bf16 v[98:101], v[162:165], v[212:215], v[98:101]
	v_mfma_f32_16x16x32_bf16 v[90:93], v[170:173], v[212:215], v[90:93]
	v_mfma_f32_16x16x32_bf16 v[82:85], v[162:165], v[220:223], v[82:85]
	v_mfma_f32_16x16x32_bf16 v[74:77], v[170:173], v[220:223], v[74:77]
	s_setprio 0
	s_setprio 1
	v_mfma_f32_16x16x32_bf16 v[118:121], v[174:177], v[192:195], v[118:121]
	v_mfma_f32_16x16x32_bf16 v[114:117], v[184:187], v[192:195], v[114:117]
	v_mfma_f32_16x16x32_bf16 v[102:105], v[174:177], v[200:203], v[102:105]
	v_mfma_f32_16x16x32_bf16 v[94:97], v[184:187], v[200:203], v[94:97]
	v_mfma_f32_16x16x32_bf16 v[86:89], v[174:177], v[208:211], v[86:89]
	v_mfma_f32_16x16x32_bf16 v[78:81], v[184:187], v[208:211], v[78:81]
	v_mfma_f32_16x16x32_bf16 v[70:73], v[174:177], v[216:219], v[70:73]
	v_mfma_f32_16x16x32_bf16 v[66:69], v[184:187], v[216:219], v[66:69]
	v_mfma_f32_16x16x32_bf16 v[118:121], v[178:181], v[196:199], v[118:121]
	v_mfma_f32_16x16x32_bf16 v[114:117], v[188:191], v[196:199], v[114:117]
	v_mfma_f32_16x16x32_bf16 v[102:105], v[178:181], v[204:207], v[102:105]
	v_mfma_f32_16x16x32_bf16 v[94:97], v[188:191], v[204:207], v[94:97]
	v_mfma_f32_16x16x32_bf16 v[86:89], v[178:181], v[212:215], v[86:89]
	v_mfma_f32_16x16x32_bf16 v[78:81], v[188:191], v[212:215], v[78:81]
	v_mfma_f32_16x16x32_bf16 v[70:73], v[178:181], v[220:223], v[70:73]
	v_mfma_f32_16x16x32_bf16 v[66:69], v[188:191], v[220:223], v[66:69]
	s_setprio 0
	s_barrier
; #define PG8_STAGE(bufoff, gbase, voff) do { _Pragma("unroll") for (int _i = 0; _i < 2; ++_i) \
;         __builtin_amdgcn_global_load_lds((const unsigned*)((const char*)(gbase) + (voff)[_i]), (PG8_LAS unsigned*)(lds + (bufoff) + ldsw + _i * 8192), 16, 0, 0); } while (0)
; #define PG8_LDA(dst, b, h) do { _Pragma("unroll") for (int m = 0; m < 4; ++m) _Pragma("unroll") for (int k = 0; k < 2; ++k) dst[m][k] = *(const PG8_LAS bf16x8*)(lds + PG8_SA(b, h) + aoff + m * 2048 + k * 1024); } while (0)
; #define PG8_MMA(ai, bj, At, Bt) do { __builtin_amdgcn_s_setprio(1); _Pragma("unroll") for (int m = 0; m < 4; ++m) _Pragma("unroll") for (int n = 0; n < 2; ++n) _Pragma("unroll") for (int k = 0; k < 2; ++k) \
;         acc[ai][bj][m][n] = __builtin_amdgcn_mfma_f32_16x16x32_bf16(Bt[n][k], At[m][k], acc[ai][bj][m][n], 0, 0, 0); __builtin_amdgcn_s_setprio(0); } while (0)
; #define PG8_WAIT_V(n) asm volatile("s_waitcnt vmcnt(" #n ")" ::: "memory")
; #define PG8_WAIT_L(n) asm volatile("s_waitcnt lgkmcnt(" #n ")" ::: "memory")
; #define PG8_BAR __builtin_amdgcn_s_barrier()
; #define PG8_SCHED __builtin_amdgcn_sched_barrier(0)
; template <class Epi, class Sched, bool ALIGN_EPI = false, bool SP2 = false>
; __device__ __forceinline__ void gemm_phase(PG8_LAS unsigned char* lds, const Gemm g, const Sched& S, const Epi& E) {
;     ...
;         for (int t = 0; t < nt; t += 2) {
;     ...
;             PG8_LDA(At, 1, 1); PG8_STAGE(PG8_SB(1, 0), b3, voffB); PG8_STAGE(PG8_SB(1, 1), b3 + hstep, voffB); PG8_STAGE(PG8_SA(1, 0), a3, voffA);
;             PG8_WAIT_V(8); PG8_WAIT_L(0); PG8_BAR; PG8_MMA(1, 0, At, B0); PG8_MMA(1, 1, At, B1); PG8_BAR; PG8_SCHED;
	s_add_i32 s28, s51, s30
	v_lshl_add_u64 v[224:225], v[224:225], 0, s[6:7]
	s_mov_b32 m0, s28
	ds_read_b128 v[192:195], v161 offset:49152
	ds_read_b128 v[196:199], v161 offset:50176
	ds_read_b128 v[200:203], v161 offset:51200
	ds_read_b128 v[204:207], v161 offset:52224
	ds_read_b128 v[208:211], v161 offset:53248
	ds_read_b128 v[212:215], v161 offset:54272
	ds_read_b128 v[216:219], v161 offset:55296
	ds_read_b128 v[220:223], v161 offset:56320
	global_load_lds_dwordx4 v[224:225], off
	s_add_i32 m0, s28, 0x2000
	s_add_u32 s26, s26, 0x100080
	v_lshl_add_u64 v[224:225], v[226:227], 0, s[6:7]
	s_addc_u32 s27, s27, 0
	s_add_i32 s28, s52, s30
	global_load_lds_dwordx4 v[224:225], off
	v_lshl_add_u64 v[224:225], s[26:27], 0, v[140:141]
	s_mov_b32 m0, s28
	s_nop 0
	global_load_lds_dwordx4 v[224:225], off
	v_lshl_add_u64 v[224:225], s[26:27], 0, v[136:137]
	s_add_i32 m0, s28, 0x2000
	s_nop 0
	global_load_lds_dwordx4 v[224:225], off
	v_lshl_add_u64 v[224:225], v[228:229], 0, s[6:7]
	s_mov_b32 m0, s39
	s_nop 0
	global_load_lds_dwordx4 v[224:225], off
	v_lshl_add_u64 v[224:225], v[230:231], 0, s[6:7]
	s_mov_b32 m0, s40
	s_nop 0
	global_load_lds_dwordx4 v[224:225], off
	s_waitcnt vmcnt(8)
	s_waitcnt lgkmcnt(0)
	s_barrier
	s_setprio 1
	s_waitcnt lgkmcnt(0)
	v_mfma_f32_16x16x32_bf16 v[62:65], v[154:157], v[192:195], v[62:65]
	v_mfma_f32_16x16x32_bf16 v[58:61], v[166:169], v[192:195], v[58:61]
	v_mfma_f32_16x16x32_bf16 v[50:53], v[154:157], v[200:203], v[50:53]
	v_mfma_f32_16x16x32_bf16 v[42:45], v[166:169], v[200:203], v[42:45]
	v_mfma_f32_16x16x32_bf16 v[34:37], v[154:157], v[208:211], v[34:37]
	v_mfma_f32_16x16x32_bf16 v[26:29], v[166:169], v[208:211], v[26:29]
	v_mfma_f32_16x16x32_bf16 v[18:21], v[154:157], v[216:219], v[18:21]
	v_mfma_f32_16x16x32_bf16 v[10:13], v[166:169], v[216:219], v[10:13]
	v_mfma_f32_16x16x32_bf16 v[62:65], v[162:165], v[196:199], v[62:65]
	v_mfma_f32_16x16x32_bf16 v[58:61], v[170:173], v[196:199], v[58:61]
	v_mfma_f32_16x16x32_bf16 v[50:53], v[162:165], v[204:207], v[50:53]
	v_mfma_f32_16x16x32_bf16 v[42:45], v[170:173], v[204:207], v[42:45]
	v_mfma_f32_16x16x32_bf16 v[34:37], v[162:165], v[212:215], v[34:37]
	v_mfma_f32_16x16x32_bf16 v[26:29], v[170:173], v[212:215], v[26:29]
	v_mfma_f32_16x16x32_bf16 v[18:21], v[162:165], v[220:223], v[18:21]
	v_mfma_f32_16x16x32_bf16 v[10:13], v[170:173], v[220:223], v[10:13]
	s_setprio 0
	s_setprio 1
	v_mfma_f32_16x16x32_bf16 v[54:57], v[174:177], v[192:195], v[54:57]
	v_mfma_f32_16x16x32_bf16 v[46:49], v[184:187], v[192:195], v[46:49]
	v_mfma_f32_16x16x32_bf16 v[38:41], v[174:177], v[200:203], v[38:41]
	v_mfma_f32_16x16x32_bf16 v[30:33], v[184:187], v[200:203], v[30:33]
	v_mfma_f32_16x16x32_bf16 v[22:25], v[174:177], v[208:211], v[22:25]
	v_mfma_f32_16x16x32_bf16 v[14:17], v[184:187], v[208:211], v[14:17]
	v_mfma_f32_16x16x32_bf16 v[6:9], v[174:177], v[216:219], v[6:9]
	v_mfma_f32_16x16x32_bf16 v[2:5], v[184:187], v[216:219], v[2:5]
	v_mfma_f32_16x16x32_bf16 v[54:57], v[178:181], v[196:199], v[54:57]
	v_mfma_f32_16x16x32_bf16 v[46:49], v[188:191], v[196:199], v[46:49]
	v_mfma_f32_16x16x32_bf16 v[38:41], v[178:181], v[204:207], v[38:41]
	v_mfma_f32_16x16x32_bf16 v[30:33], v[188:191], v[204:207], v[30:33]
	v_mfma_f32_16x16x32_bf16 v[22:25], v[178:181], v[212:215], v[22:25]
	v_mfma_f32_16x16x32_bf16 v[14:17], v[188:191], v[212:215], v[14:17]
	v_mfma_f32_16x16x32_bf16 v[6:9], v[178:181], v[220:223], v[6:9]
	v_mfma_f32_16x16x32_bf16 v[2:5], v[188:191], v[220:223], v[2:5]
	s_setprio 0
	s_barrier
	s_add_i32 s50, s50, 2
	s_add_u32 s24, s24, 0x100
	s_addc_u32 s25, s25, 0
	s_add_u32 s47, s47, 0x100
	s_addc_u32 s49, s49, 0
	s_cmp_gt_u32 s50, 61
	s_cbranch_scc0 .LBB0_102
	s_and_b64 vcc, exec, s[12:13]
	s_cbranch_vccz .LBB0_105
	s_barrier

; #define PG8_STAGE(bufoff, gbase, voff) do { _Pragma("unroll") for (int _i = 0; _i < 2; ++_i) \
;         __builtin_amdgcn_global_load_lds((const unsigned*)((const char*)(gbase) + (voff)[_i]), (PG8_LAS unsigned*)(lds + (bufoff) + ldsw + _i * 8192), 16, 0, 0); } while (0)
; #define PG8_LDA(dst, b, h) do { _Pragma("unroll") for (int m = 0; m < 4; ++m) _Pragma("unroll") for (int k = 0; k < 2; ++k) dst[m][k] = *(const PG8_LAS bf16x8*)(lds + PG8_SA(b, h) + aoff + m * 2048 + k * 1024); } while (0)
; #define PG8_LDB(dst, b, h) do { _Pragma("unroll") for (int n = 0; n < 2; ++n) _Pragma("unroll") for (int k = 0; k < 2; ++k) dst[n][k] = *(const PG8_LAS bf16x8*)(lds + PG8_SB(b, h) + boff + n * 2048 + k * 1024); } while (0)
; #define PG8_MMA(ai, bj, At, Bt) do { __builtin_amdgcn_s_setprio(1); _Pragma("unroll") for (int m = 0; m < 4; ++m) _Pragma("unroll") for (int n = 0; n < 2; ++n) _Pragma("unroll") for (int k = 0; k < 2; ++k) \
;         acc[ai][bj][m][n] = __builtin_amdgcn_mfma_f32_16x16x32_bf16(Bt[n][k], At[m][k], acc[ai][bj][m][n], 0, 0, 0); __builtin_amdgcn_s_setprio(0); } while (0)
; #define PG8_WAIT_V(n) asm volatile("s_waitcnt vmcnt(" #n ")" ::: "memory")
; #define PG8_WAIT_L(n) asm volatile("s_waitcnt lgkmcnt(" #n ")" ::: "memory")
; #define PG8_BAR __builtin_amdgcn_s_barrier()
; #define PG8_SCHED __builtin_amdgcn_sched_barrier(0)
; template <class Epi, class Sched, bool ALIGN_EPI = false, bool SP2 = false>
; __device__ __forceinline__ void gemm_phase(PG8_LAS unsigned char* lds, const Gemm g, const Sched& S, const Epi& E) {
;     ...
;             PG8_LDB(B0, 0, 0); PG8_LDB(B1, 0, 1); PG8_SCHED; PG8_LDA(At, 0, 0); PG8_STAGE(PG8_SA(1, 1), a1 + hstep, voffA);
;             PG8_WAIT_V(8); PG8_WAIT_L(0); PG8_BAR; PG8_MMA(0, 0, At, B0); PG8_MMA(0, 1, At, B1); PG8_BAR; PG8_SCHED;
;             PG8_LDA(At, 0, 1); PG8_STAGE(PG8_SB(0, 0), b2, voffB); PG8_STAGE(PG8_SB(0, 1), b2 + hstep, voffB); PG8_STAGE(PG8_SA(0, 0), a2, voffA);
;             PG8_WAIT_V(8); PG8_WAIT_L(0); PG8_BAR; PG8_MMA(1, 0, At, B0); PG8_MMA(1, 1, At, B1); PG8_BAR; PG8_SCHED;
.LBB0_563:
	ds_read_b128 v[146:149], v154
	ds_read_b128 v[158:161], v154 offset:1024
	ds_read_b128 v[162:165], v154 offset:2048
	ds_read_b128 v[166:169], v154 offset:3072
	ds_read_b128 v[170:173], v155
	ds_read_b128 v[174:177], v155 offset:1024
	ds_read_b128 v[178:181], v155 offset:2048
	ds_read_b128 v[184:187], v155 offset:3072
	s_add_u32 s30, s28, 0xffe00080
	s_addc_u32 s31, s29, -1
	s_cmpk_eq_i32 s51, 0x7c
	s_cselect_b32 s35, s21, s31
	s_cselect_b32 s34, s47, s30
	s_cselect_b32 s31, s19, s50
	s_cselect_b32 s30, s48, s49
	v_lshl_add_u64 v[150:151], s[28:29], 0, v[138:139]
	s_add_i32 m0, s27, 0xc000
	ds_read_b128 v[188:191], v156
	ds_read_b128 v[192:195], v156 offset:1024
	ds_read_b128 v[196:199], v156 offset:2048
	ds_read_b128 v[200:203], v156 offset:3072
	ds_read_b128 v[204:207], v156 offset:4096
	ds_read_b128 v[208:211], v156 offset:5120
	ds_read_b128 v[212:215], v156 offset:6144
	ds_read_b128 v[216:219], v156 offset:7168
	global_load_lds_dwordx4 v[150:151], off
	v_lshl_add_u64 v[150:151], s[28:29], 0, v[140:141]
	s_add_i32 m0, s27, 0xe000
	s_nop 0
	global_load_lds_dwordx4 v[150:151], off
	s_waitcnt vmcnt(8)
	s_waitcnt lgkmcnt(0)
	s_barrier
	s_setprio 1
	s_waitcnt lgkmcnt(0)
	v_mfma_f32_16x16x32_bf16 v[126:129], v[146:149], v[188:191], v[126:129]
	v_mfma_f32_16x16x32_bf16 v[122:125], v[162:165], v[188:191], v[122:125]
	v_mfma_f32_16x16x32_bf16 v[110:113], v[146:149], v[196:199], v[110:113]
	v_mfma_f32_16x16x32_bf16 v[106:109], v[162:165], v[196:199], v[106:109]
	v_mfma_f32_16x16x32_bf16 v[94:97], v[146:149], v[204:207], v[94:97]
	v_mfma_f32_16x16x32_bf16 v[90:93], v[162:165], v[204:207], v[90:93]
	v_mfma_f32_16x16x32_bf16 v[78:81], v[146:149], v[212:215], v[78:81]
	v_mfma_f32_16x16x32_bf16 v[74:77], v[162:165], v[212:215], v[74:77]
	v_mfma_f32_16x16x32_bf16 v[126:129], v[158:161], v[192:195], v[126:129]
	v_mfma_f32_16x16x32_bf16 v[122:125], v[166:169], v[192:195], v[122:125]
	v_mfma_f32_16x16x32_bf16 v[110:113], v[158:161], v[200:203], v[110:113]
	v_mfma_f32_16x16x32_bf16 v[106:109], v[166:169], v[200:203], v[106:109]
	v_mfma_f32_16x16x32_bf16 v[94:97], v[158:161], v[208:211], v[94:97]
	v_mfma_f32_16x16x32_bf16 v[90:93], v[166:169], v[208:211], v[90:93]
	v_mfma_f32_16x16x32_bf16 v[78:81], v[158:161], v[216:219], v[78:81]
	v_mfma_f32_16x16x32_bf16 v[74:77], v[166:169], v[216:219], v[74:77]
	s_setprio 0
	s_setprio 1
	v_mfma_f32_16x16x32_bf16 v[118:121], v[170:173], v[188:191], v[118:121]
	v_mfma_f32_16x16x32_bf16 v[114:117], v[178:181], v[188:191], v[114:117]
	v_mfma_f32_16x16x32_bf16 v[102:105], v[170:173], v[196:199], v[102:105]
	v_mfma_f32_16x16x32_bf16 v[98:101], v[178:181], v[196:199], v[98:101]
	v_mfma_f32_16x16x32_bf16 v[86:89], v[170:173], v[204:207], v[86:89]
	v_mfma_f32_16x16x32_bf16 v[82:85], v[178:181], v[204:207], v[82:85]
	v_mfma_f32_16x16x32_bf16 v[70:73], v[170:173], v[212:215], v[70:73]
	v_mfma_f32_16x16x32_bf16 v[66:69], v[178:181], v[212:215], v[66:69]
	v_mfma_f32_16x16x32_bf16 v[118:121], v[174:177], v[192:195], v[118:121]
	v_mfma_f32_16x16x32_bf16 v[114:117], v[184:187], v[192:195], v[114:117]
	v_mfma_f32_16x16x32_bf16 v[102:105], v[174:177], v[200:203], v[102:105]
	v_mfma_f32_16x16x32_bf16 v[98:101], v[184:187], v[200:203], v[98:101]
	v_mfma_f32_16x16x32_bf16 v[86:89], v[174:177], v[208:211], v[86:89]
	v_mfma_f32_16x16x32_bf16 v[82:85], v[184:187], v[208:211], v[82:85]
	v_mfma_f32_16x16x32_bf16 v[70:73], v[174:177], v[216:219], v[70:73]
	v_mfma_f32_16x16x32_bf16 v[66:69], v[184:187], v[216:219], v[66:69]
	s_setprio 0
	s_barrier
	s_nop 0
	s_add_i32 s52, s44, s36
	v_lshl_add_u64 v[150:151], s[30:31], 0, v[132:133]
	s_mov_b32 m0, s52
	ds_read_b128 v[188:191], v156 offset:16384
	ds_read_b128 v[192:195], v156 offset:17408
	ds_read_b128 v[196:199], v156 offset:18432
	ds_read_b128 v[200:203], v156 offset:19456
	ds_read_b128 v[204:207], v156 offset:20480
	ds_read_b128 v[208:211], v156 offset:21504
	ds_read_b128 v[212:215], v156 offset:22528
	ds_read_b128 v[216:219], v156 offset:23552
	global_load_lds_dwordx4 v[150:151], off
	s_add_i32 m0, s52, 0x2000
	s_add_u32 s52, s30, 0x200000
	v_lshl_add_u64 v[220:221], s[30:31], 0, v[136:137]
	s_addc_u32 s53, s31, 0
	s_add_i32 s54, s45, s36
	global_load_lds_dwordx4 v[220:221], off
	v_lshl_add_u64 v[222:223], s[52:53], 0, v[132:133]
	s_mov_b32 m0, s54
	v_lshl_add_u64 v[224:225], s[34:35], 0, v[134:135]
	global_load_lds_dwordx4 v[222:223], off
	v_lshl_add_u64 v[222:223], s[52:53], 0, v[136:137]
	s_add_i32 m0, s54, 0x2000
	s_nop 0
	global_load_lds_dwordx4 v[222:223], off
	v_lshl_add_u64 v[222:223], s[34:35], 0, v[130:131]
	s_mov_b32 m0, s27
	s_nop 0
	global_load_lds_dwordx4 v[222:223], off
	s_mov_b32 m0, s37
	s_nop 0
	global_load_lds_dwordx4 v[224:225], off
	s_waitcnt vmcnt(8)
	s_waitcnt lgkmcnt(0)
	s_barrier
; #define PG8_STAGE(bufoff, gbase, voff) do { _Pragma("unroll") for (int _i = 0; _i < 2; ++_i) \
;         __builtin_amdgcn_global_load_lds((const unsigned*)((const char*)(gbase) + (voff)[_i]), (PG8_LAS unsigned*)(lds + (bufoff) + ldsw + _i * 8192), 16, 0, 0); } while (0)
; #define PG8_LDA(dst, b, h) do { _Pragma("unroll") for (int m = 0; m < 4; ++m) _Pragma("unroll") for (int k = 0; k < 2; ++k) dst[m][k] = *(const PG8_LAS bf16x8*)(lds + PG8_SA(b, h) + aoff + m * 2048 + k * 1024); } while (0)
; #define PG8_LDB(dst, b, h) do { _Pragma("unroll") for (int n = 0; n < 2; ++n) _Pragma("unroll") for (int k = 0; k < 2; ++k) dst[n][k] = *(const PG8_LAS bf16x8*)(lds + PG8_SB(b, h) + boff + n * 2048 + k * 1024); } while (0)
; #define PG8_MMA(ai, bj, At, Bt) do { __builtin_amdgcn_s_setprio(1); _Pragma("unroll") for (int m = 0; m < 4; ++m) _Pragma("unroll") for (int n = 0; n < 2; ++n) _Pragma("unroll") for (int k = 0; k < 2; ++k) \
;         acc[ai][bj][m][n] = __builtin_amdgcn_mfma_f32_16x16x32_bf16(Bt[n][k], At[m][k], acc[ai][bj][m][n], 0, 0, 0); __builtin_amdgcn_s_setprio(0); } while (0)
; #define PG8_WAIT_V(n) asm volatile("s_waitcnt vmcnt(" #n ")" ::: "memory")
; #define PG8_WAIT_L(n) asm volatile("s_waitcnt lgkmcnt(" #n ")" ::: "memory")
; #define PG8_BAR __builtin_amdgcn_s_barrier()
; #define PG8_SCHED __builtin_amdgcn_sched_barrier(0)
; template <class Epi, class Sched, bool ALIGN_EPI = false, bool SP2 = false>
; __device__ __forceinline__ void gemm_phase(PG8_LAS unsigned char* lds, const Gemm g, const Sched& S, const Epi& E) {
;     ...
;             PG8_WAIT_V(8); PG8_WAIT_L(0); PG8_BAR; PG8_MMA(1, 0, At, B0); PG8_MMA(1, 1, At, B1); PG8_BAR; PG8_SCHED;
;             PG8_LDB(B0, 1, 0); PG8_LDB(B1, 1, 1); PG8_SCHED; PG8_LDA(At, 1, 0); PG8_STAGE(PG8_SA(0, 1), a2 + hstep, voffA);
;             PG8_WAIT_V(8); PG8_WAIT_L(0); PG8_BAR; PG8_MMA(0, 0, At, B0); PG8_MMA(0, 1, At, B1); PG8_BAR; PG8_SCHED;
	s_setprio 1
	s_waitcnt lgkmcnt(0)
	v_mfma_f32_16x16x32_bf16 v[62:65], v[146:149], v[188:191], v[62:65]
	v_mfma_f32_16x16x32_bf16 v[58:61], v[162:165], v[188:191], v[58:61]
	v_mfma_f32_16x16x32_bf16 v[46:49], v[146:149], v[196:199], v[46:49]
	v_mfma_f32_16x16x32_bf16 v[42:45], v[162:165], v[196:199], v[42:45]
	v_mfma_f32_16x16x32_bf16 v[30:33], v[146:149], v[204:207], v[30:33]
	v_mfma_f32_16x16x32_bf16 v[26:29], v[162:165], v[204:207], v[26:29]
	v_mfma_f32_16x16x32_bf16 v[14:17], v[146:149], v[212:215], v[14:17]
	v_mfma_f32_16x16x32_bf16 v[10:13], v[162:165], v[212:215], v[10:13]
	v_mfma_f32_16x16x32_bf16 v[62:65], v[158:161], v[192:195], v[62:65]
	v_mfma_f32_16x16x32_bf16 v[58:61], v[166:169], v[192:195], v[58:61]
	v_mfma_f32_16x16x32_bf16 v[46:49], v[158:161], v[200:203], v[46:49]
	v_mfma_f32_16x16x32_bf16 v[42:45], v[166:169], v[200:203], v[42:45]
	v_mfma_f32_16x16x32_bf16 v[30:33], v[158:161], v[208:211], v[30:33]
	v_mfma_f32_16x16x32_bf16 v[26:29], v[166:169], v[208:211], v[26:29]
	v_mfma_f32_16x16x32_bf16 v[14:17], v[158:161], v[216:219], v[14:17]
	v_mfma_f32_16x16x32_bf16 v[10:13], v[166:169], v[216:219], v[10:13]
	s_setprio 0
	s_setprio 1
	v_mfma_f32_16x16x32_bf16 v[54:57], v[170:173], v[188:191], v[54:57]
	v_mfma_f32_16x16x32_bf16 v[50:53], v[178:181], v[188:191], v[50:53]
	v_mfma_f32_16x16x32_bf16 v[38:41], v[170:173], v[196:199], v[38:41]
	v_mfma_f32_16x16x32_bf16 v[34:37], v[178:181], v[196:199], v[34:37]
	v_mfma_f32_16x16x32_bf16 v[22:25], v[170:173], v[204:207], v[22:25]
	v_mfma_f32_16x16x32_bf16 v[18:21], v[178:181], v[204:207], v[18:21]
	v_mfma_f32_16x16x32_bf16 v[6:9], v[170:173], v[212:215], v[6:9]
	v_mfma_f32_16x16x32_bf16 v[2:5], v[178:181], v[212:215], v[2:5]
	v_mfma_f32_16x16x32_bf16 v[54:57], v[174:177], v[192:195], v[54:57]
	v_mfma_f32_16x16x32_bf16 v[50:53], v[184:187], v[192:195], v[50:53]
	v_mfma_f32_16x16x32_bf16 v[38:41], v[174:177], v[200:203], v[38:41]
	v_mfma_f32_16x16x32_bf16 v[34:37], v[184:187], v[200:203], v[34:37]
	v_mfma_f32_16x16x32_bf16 v[22:25], v[174:177], v[208:211], v[22:25]
	v_mfma_f32_16x16x32_bf16 v[18:21], v[184:187], v[208:211], v[18:21]
	v_mfma_f32_16x16x32_bf16 v[6:9], v[174:177], v[216:219], v[6:9]
	v_mfma_f32_16x16x32_bf16 v[2:5], v[184:187], v[216:219], v[2:5]
	s_setprio 0
	s_barrier
	s_nop 0
	s_add_i32 s52, 0, 0x18000
	v_add_u32_e32 v157, s52, v152
	s_add_i32 s53, 0, 0x1c000
	ds_read_b128 v[146:149], v157
	ds_read_b128 v[158:161], v157 offset:1024
	ds_read_b128 v[162:165], v157 offset:2048
	ds_read_b128 v[166:169], v157 offset:3072
	v_add_u32_e32 v157, s53, v152
	ds_read_b128 v[170:173], v157
	ds_read_b128 v[174:177], v157 offset:1024
	ds_read_b128 v[178:181], v157 offset:2048
	ds_read_b128 v[184:187], v157 offset:3072
	s_add_u32 s34, s34, 0x200000
	s_addc_u32 s35, s35, 0
	s_mov_b32 m0, s38
	v_lshl_add_u64 v[226:227], s[34:35], 0, v[130:131]
	ds_read_b128 v[188:191], v156 offset:32768
	ds_read_b128 v[192:195], v156 offset:33792
	ds_read_b128 v[196:199], v156 offset:34816
	ds_read_b128 v[200:203], v156 offset:35840
	ds_read_b128 v[204:207], v156 offset:36864
	ds_read_b128 v[208:211], v156 offset:37888
	ds_read_b128 v[212:215], v156 offset:38912
	ds_read_b128 v[216:219], v156 offset:39936
	global_load_lds_dwordx4 v[226:227], off
	v_lshl_add_u64 v[226:227], s[34:35], 0, v[134:135]
	s_mov_b32 m0, s39
	s_nop 0
	global_load_lds_dwordx4 v[226:227], off
	s_waitcnt vmcnt(8)
	s_waitcnt lgkmcnt(0)
	s_barrier
	s_setprio 1
	s_waitcnt lgkmcnt(0)
	v_mfma_f32_16x16x32_bf16 v[126:129], v[146:149], v[188:191], v[126:129]
	v_mfma_f32_16x16x32_bf16 v[122:125], v[162:165], v[188:191], v[122:125]
	v_mfma_f32_16x16x32_bf16 v[110:113], v[146:149], v[196:199], v[110:113]
	v_mfma_f32_16x16x32_bf16 v[106:109], v[162:165], v[196:199], v[106:109]
	v_mfma_f32_16x16x32_bf16 v[94:97], v[146:149], v[204:207], v[94:97]
	v_mfma_f32_16x16x32_bf16 v[90:93], v[162:165], v[204:207], v[90:93]
	v_mfma_f32_16x16x32_bf16 v[78:81], v[146:149], v[212:215], v[78:81]
	v_mfma_f32_16x16x32_bf16 v[74:77], v[162:165], v[212:215], v[74:77]
	v_mfma_f32_16x16x32_bf16 v[126:129], v[158:161], v[192:195], v[126:129]
	v_mfma_f32_16x16x32_bf16 v[122:125], v[166:169], v[192:195], v[122:125]
	v_mfma_f32_16x16x32_bf16 v[110:113], v[158:161], v[200:203], v[110:113]
	v_mfma_f32_16x16x32_bf16 v[106:109], v[166:169], v[200:203], v[106:109]
	v_mfma_f32_16x16x32_bf16 v[94:97], v[158:161], v[208:211], v[94:97]
	v_mfma_f32_16x16x32_bf16 v[90:93], v[166:169], v[208:211], v[90:93]
	v_mfma_f32_16x16x32_bf16 v[78:81], v[158:161], v[216:219], v[78:81]
	v_mfma_f32_16x16x32_bf16 v[74:77], v[166:169], v[216:219], v[74:77]
	s_setprio 0
	s_setprio 1
	v_mfma_f32_16x16x32_bf16 v[118:121], v[170:173], v[188:191], v[118:121]
	v_mfma_f32_16x16x32_bf16 v[114:117], v[178:181], v[188:191], v[114:117]
	v_mfma_f32_16x16x32_bf16 v[102:105], v[170:173], v[196:199], v[102:105]
	v_mfma_f32_16x16x32_bf16 v[98:101], v[178:181], v[196:199], v[98:101]
	v_mfma_f32_16x16x32_bf16 v[86:89], v[170:173], v[204:207], v[86:89]
	v_mfma_f32_16x16x32_bf16 v[82:85], v[178:181], v[204:207], v[82:85]
	v_mfma_f32_16x16x32_bf16 v[70:73], v[170:173], v[212:215], v[70:73]
	v_mfma_f32_16x16x32_bf16 v[66:69], v[178:181], v[212:215], v[66:69]
	v_mfma_f32_16x16x32_bf16 v[118:121], v[174:177], v[192:195], v[118:121]
	v_mfma_f32_16x16x32_bf16 v[114:117], v[184:187], v[192:195], v[114:117]
	v_mfma_f32_16x16x32_bf16 v[102:105], v[174:177], v[200:203], v[102:105]
	v_mfma_f32_16x16x32_bf16 v[98:101], v[184:187], v[200:203], v[98:101]
	v_mfma_f32_16x16x32_bf16 v[86:89], v[174:177], v[208:211], v[86:89]
	v_mfma_f32_16x16x32_bf16 v[82:85], v[184:187], v[208:211], v[82:85]
	v_mfma_f32_16x16x32_bf16 v[70:73], v[174:177], v[216:219], v[70:73]
	v_mfma_f32_16x16x32_bf16 v[66:69], v[184:187], v[216:219], v[66:69]
	s_setprio 0
	s_barrier
; #define PG8_STAGE(bufoff, gbase, voff) do { _Pragma("unroll") for (int _i = 0; _i < 2; ++_i) \
;         __builtin_amdgcn_global_load_lds((const unsigned*)((const char*)(gbase) + (voff)[_i]), (PG8_LAS unsigned*)(lds + (bufoff) + ldsw + _i * 8192), 16, 0, 0); } while (0)
; #define PG8_LDA(dst, b, h) do { _Pragma("unroll") for (int m = 0; m < 4; ++m) _Pragma("unroll") for (int k = 0; k < 2; ++k) dst[m][k] = *(const PG8_LAS bf16x8*)(lds + PG8_SA(b, h) + aoff + m * 2048 + k * 1024); } while (0)
; #define PG8_MMA(ai, bj, At, Bt) do { __builtin_amdgcn_s_setprio(1); _Pragma("unroll") for (int m = 0; m < 4; ++m) _Pragma("unroll") for (int n = 0; n < 2; ++n) _Pragma("unroll") for (int k = 0; k < 2; ++k) \
;         acc[ai][bj][m][n] = __builtin_amdgcn_mfma_f32_16x16x32_bf16(Bt[n][k], At[m][k], acc[ai][bj][m][n], 0, 0, 0); __builtin_amdgcn_s_setprio(0); } while (0)
; #define PG8_WAIT_V(n) asm volatile("s_waitcnt vmcnt(" #n ")" ::: "memory")
; #define PG8_WAIT_L(n) asm volatile("s_waitcnt lgkmcnt(" #n ")" ::: "memory")
; #define PG8_BAR __builtin_amdgcn_s_barrier()
; #define PG8_SCHED __builtin_amdgcn_sched_barrier(0)
; template <class Epi, class Sched, bool ALIGN_EPI = false, bool SP2 = false>
; __device__ __forceinline__ void gemm_phase(PG8_LAS unsigned char* lds, const Gemm g, const Sched& S, const Epi& E) {
;     ...
;         for (int t = 0; t < nt; t += 2) {
;     ...
;             PG8_LDA(At, 1, 1); PG8_STAGE(PG8_SB(1, 0), b3, voffB); PG8_STAGE(PG8_SB(1, 1), b3 + hstep, voffB); PG8_STAGE(PG8_SA(1, 0), a3, voffA);
;             PG8_WAIT_V(8); PG8_WAIT_L(0); PG8_BAR; PG8_MMA(1, 0, At, B0); PG8_MMA(1, 1, At, B1); PG8_BAR; PG8_SCHED;
	s_add_i32 s34, s52, s36
	v_lshl_add_u64 v[150:151], v[150:151], 0, s[2:3]
	s_mov_b32 m0, s34
	ds_read_b128 v[188:191], v156 offset:49152
	ds_read_b128 v[192:195], v156 offset:50176
	ds_read_b128 v[196:199], v156 offset:51200
	ds_read_b128 v[200:203], v156 offset:52224
	ds_read_b128 v[204:207], v156 offset:53248
	ds_read_b128 v[208:211], v156 offset:54272
	ds_read_b128 v[212:215], v156 offset:55296
	ds_read_b128 v[216:219], v156 offset:56320
	global_load_lds_dwordx4 v[150:151], off
	s_add_i32 m0, s34, 0x2000
	s_add_u32 s30, s30, 0x200080
	v_lshl_add_u64 v[150:151], v[220:221], 0, s[2:3]
	s_addc_u32 s31, s31, 0
	s_add_i32 s34, s53, s36
	global_load_lds_dwordx4 v[150:151], off
	v_lshl_add_u64 v[150:151], s[30:31], 0, v[132:133]
	s_mov_b32 m0, s34
	s_nop 0
	global_load_lds_dwordx4 v[150:151], off
	v_lshl_add_u64 v[150:151], s[30:31], 0, v[136:137]
	s_add_i32 m0, s34, 0x2000
	s_nop 0
	global_load_lds_dwordx4 v[150:151], off
	v_lshl_add_u64 v[150:151], v[222:223], 0, s[2:3]
	s_mov_b32 m0, s41
	s_nop 0
	global_load_lds_dwordx4 v[150:151], off
	v_lshl_add_u64 v[150:151], v[224:225], 0, s[2:3]
	s_mov_b32 m0, s42
	s_nop 0
	global_load_lds_dwordx4 v[150:151], off
	s_waitcnt vmcnt(8)
	s_waitcnt lgkmcnt(0)
	s_barrier
	s_setprio 1
	s_waitcnt lgkmcnt(0)
	v_mfma_f32_16x16x32_bf16 v[62:65], v[146:149], v[188:191], v[62:65]
	v_mfma_f32_16x16x32_bf16 v[58:61], v[162:165], v[188:191], v[58:61]
	v_mfma_f32_16x16x32_bf16 v[46:49], v[146:149], v[196:199], v[46:49]
	v_mfma_f32_16x16x32_bf16 v[42:45], v[162:165], v[196:199], v[42:45]
	v_mfma_f32_16x16x32_bf16 v[30:33], v[146:149], v[204:207], v[30:33]
	v_mfma_f32_16x16x32_bf16 v[26:29], v[162:165], v[204:207], v[26:29]
	v_mfma_f32_16x16x32_bf16 v[14:17], v[146:149], v[212:215], v[14:17]
	v_mfma_f32_16x16x32_bf16 v[10:13], v[162:165], v[212:215], v[10:13]
	v_mfma_f32_16x16x32_bf16 v[62:65], v[158:161], v[192:195], v[62:65]
	v_mfma_f32_16x16x32_bf16 v[58:61], v[166:169], v[192:195], v[58:61]
	v_mfma_f32_16x16x32_bf16 v[46:49], v[158:161], v[200:203], v[46:49]
	v_mfma_f32_16x16x32_bf16 v[42:45], v[166:169], v[200:203], v[42:45]
	v_mfma_f32_16x16x32_bf16 v[30:33], v[158:161], v[208:211], v[30:33]
	v_mfma_f32_16x16x32_bf16 v[26:29], v[166:169], v[208:211], v[26:29]
	v_mfma_f32_16x16x32_bf16 v[14:17], v[158:161], v[216:219], v[14:17]
	v_mfma_f32_16x16x32_bf16 v[10:13], v[166:169], v[216:219], v[10:13]
	s_setprio 0
	s_setprio 1
	v_mfma_f32_16x16x32_bf16 v[54:57], v[170:173], v[188:191], v[54:57]
	v_mfma_f32_16x16x32_bf16 v[50:53], v[178:181], v[188:191], v[50:53]
	v_mfma_f32_16x16x32_bf16 v[38:41], v[170:173], v[196:199], v[38:41]
	v_mfma_f32_16x16x32_bf16 v[34:37], v[178:181], v[196:199], v[34:37]
	v_mfma_f32_16x16x32_bf16 v[22:25], v[170:173], v[204:207], v[22:25]
	v_mfma_f32_16x16x32_bf16 v[18:21], v[178:181], v[204:207], v[18:21]
	v_mfma_f32_16x16x32_bf16 v[6:9], v[170:173], v[212:215], v[6:9]
	v_mfma_f32_16x16x32_bf16 v[2:5], v[178:181], v[212:215], v[2:5]
	v_mfma_f32_16x16x32_bf16 v[54:57], v[174:177], v[192:195], v[54:57]
	v_mfma_f32_16x16x32_bf16 v[50:53], v[184:187], v[192:195], v[50:53]
	v_mfma_f32_16x16x32_bf16 v[38:41], v[174:177], v[200:203], v[38:41]
	v_mfma_f32_16x16x32_bf16 v[34:37], v[184:187], v[200:203], v[34:37]
	v_mfma_f32_16x16x32_bf16 v[22:25], v[174:177], v[208:211], v[22:25]
	v_mfma_f32_16x16x32_bf16 v[18:21], v[184:187], v[208:211], v[18:21]
	v_mfma_f32_16x16x32_bf16 v[6:9], v[174:177], v[216:219], v[6:9]
	v_mfma_f32_16x16x32_bf16 v[2:5], v[184:187], v[216:219], v[2:5]
	s_setprio 0
	s_barrier
	s_add_i32 s51, s51, 2
	s_add_u32 s28, s28, 0x100
	s_addc_u32 s29, s29, 0
	s_add_u32 s49, s49, 0x100
	s_addc_u32 s50, s50, 0
	s_cmpk_gt_u32 s51, 0x7d
	s_cbranch_scc0 .LBB0_563
	s_and_b64 vcc, exec, s[8:9]
	s_cbranch_vccz .LBB0_566
	s_barrier

; #define PG8_STAGE(bufoff, gbase, voff) do { _Pragma("unroll") for (int _i = 0; _i < 2; ++_i) \
;         __builtin_amdgcn_global_load_lds((const unsigned*)((const char*)(gbase) + (voff)[_i]), (PG8_LAS unsigned*)(lds + (bufoff) + ldsw + _i * 8192), 16, 0, 0); } while (0)
; #define PG8_LDA(dst, b, h) do { _Pragma("unroll") for (int m = 0; m < 4; ++m) _Pragma("unroll") for (int k = 0; k < 2; ++k) dst[m][k] = *(const PG8_LAS bf16x8*)(lds + PG8_SA(b, h) + aoff + m * 2048 + k * 1024); } while (0)
; #define PG8_LDB(dst, b, h) do { _Pragma("unroll") for (int n = 0; n < 2; ++n) _Pragma("unroll") for (int k = 0; k < 2; ++k) dst[n][k] = *(const PG8_LAS bf16x8*)(lds + PG8_SB(b, h) + boff + n * 2048 + k * 1024); } while (0)
; #define PG8_MMA(ai, bj, At, Bt) do { __builtin_amdgcn_s_setprio(1); _Pragma("unroll") for (int m = 0; m < 4; ++m) _Pragma("unroll") for (int n = 0; n < 2; ++n) _Pragma("unroll") for (int k = 0; k < 2; ++k) \
;         acc[ai][bj][m][n] = __builtin_amdgcn_mfma_f32_16x16x32_bf16(Bt[n][k], At[m][k], acc[ai][bj][m][n], 0, 0, 0); __builtin_amdgcn_s_setprio(0); } while (0)
; #define PG8_WAIT_V(n) asm volatile("s_waitcnt vmcnt(" #n ")" ::: "memory")
; #define PG8_WAIT_L(n) asm volatile("s_waitcnt lgkmcnt(" #n ")" ::: "memory")
; #define PG8_BAR __builtin_amdgcn_s_barrier()
; #define PG8_SCHED __builtin_amdgcn_sched_barrier(0)
; template <class Epi, class Sched, bool ALIGN_EPI = false, bool SP2 = false>
; __device__ __forceinline__ void gemm_phase(PG8_LAS unsigned char* lds, const Gemm g, const Sched& S, const Epi& E) {
;     ...
;             PG8_LDB(B0, 0, 0); PG8_LDB(B1, 0, 1); PG8_SCHED; PG8_LDA(At, 0, 0); PG8_STAGE(PG8_SA(1, 1), a1 + hstep, voffA);
;             PG8_WAIT_V(8); PG8_WAIT_L(0); PG8_BAR; PG8_MMA(0, 0, At, B0); PG8_MMA(0, 1, At, B1); PG8_BAR; PG8_SCHED;
;             PG8_LDA(At, 0, 1); PG8_STAGE(PG8_SB(0, 0), b2, voffB); PG8_STAGE(PG8_SB(0, 1), b2 + hstep, voffB); PG8_STAGE(PG8_SA(0, 0), a2, voffA);
;             PG8_WAIT_V(8); PG8_WAIT_L(0); PG8_BAR; PG8_MMA(1, 0, At, B0); PG8_MMA(1, 1, At, B1); PG8_BAR; PG8_SCHED;
.LBB0_707:
	ds_read_b128 v[142:145], v151
	ds_read_b128 v[154:157], v151 offset:1024
	ds_read_b128 v[158:161], v151 offset:2048
	ds_read_b128 v[162:165], v151 offset:3072
	ds_read_b128 v[166:169], v152
	ds_read_b128 v[170:173], v152 offset:1024
	ds_read_b128 v[174:177], v152 offset:2048
	ds_read_b128 v[178:181], v152 offset:3072
	s_add_u32 s34, s30, 0xfff00080
	s_addc_u32 s35, s31, -1
	s_cmp_eq_u32 s61, 60
	s_cselect_b32 s37, s25, s35
	s_cselect_b32 s36, s57, s34
	s_cselect_b32 s35, s23, s60
	s_cselect_b32 s34, s58, s59
	v_lshl_add_u64 v[216:217], s[30:31], 0, v[134:135]
	s_add_i32 m0, s42, 0xc000
	ds_read_b128 v[184:187], v153
	ds_read_b128 v[188:191], v153 offset:1024
	ds_read_b128 v[192:195], v153 offset:2048
	ds_read_b128 v[196:199], v153 offset:3072
	ds_read_b128 v[200:203], v153 offset:4096
	ds_read_b128 v[204:207], v153 offset:5120
	ds_read_b128 v[208:211], v153 offset:6144
	ds_read_b128 v[212:215], v153 offset:7168
	global_load_lds_dwordx4 v[216:217], off
	v_lshl_add_u64 v[216:217], s[30:31], 0, v[136:137]
	s_add_i32 m0, s42, 0xe000
	s_nop 0
	global_load_lds_dwordx4 v[216:217], off
	s_waitcnt vmcnt(8)
	s_waitcnt lgkmcnt(0)
	s_barrier
	s_setprio 1
	s_waitcnt lgkmcnt(0)
	v_mfma_f32_16x16x32_bf16 v[126:129], v[142:145], v[184:187], v[126:129]
	v_mfma_f32_16x16x32_bf16 v[122:125], v[158:161], v[184:187], v[122:125]
	v_mfma_f32_16x16x32_bf16 v[110:113], v[142:145], v[192:195], v[110:113]
	v_mfma_f32_16x16x32_bf16 v[106:109], v[158:161], v[192:195], v[106:109]
	v_mfma_f32_16x16x32_bf16 v[94:97], v[142:145], v[200:203], v[94:97]
	v_mfma_f32_16x16x32_bf16 v[90:93], v[158:161], v[200:203], v[90:93]
	v_mfma_f32_16x16x32_bf16 v[86:89], v[142:145], v[208:211], v[86:89]
	v_mfma_f32_16x16x32_bf16 v[78:81], v[158:161], v[208:211], v[78:81]
	v_mfma_f32_16x16x32_bf16 v[126:129], v[154:157], v[188:191], v[126:129]
	v_mfma_f32_16x16x32_bf16 v[122:125], v[162:165], v[188:191], v[122:125]
	v_mfma_f32_16x16x32_bf16 v[110:113], v[154:157], v[196:199], v[110:113]
	v_mfma_f32_16x16x32_bf16 v[106:109], v[162:165], v[196:199], v[106:109]
	v_mfma_f32_16x16x32_bf16 v[94:97], v[154:157], v[204:207], v[94:97]
	v_mfma_f32_16x16x32_bf16 v[90:93], v[162:165], v[204:207], v[90:93]
	v_mfma_f32_16x16x32_bf16 v[86:89], v[154:157], v[212:215], v[86:89]
	v_mfma_f32_16x16x32_bf16 v[78:81], v[162:165], v[212:215], v[78:81]
	s_setprio 0
	s_setprio 1
	v_mfma_f32_16x16x32_bf16 v[118:121], v[166:169], v[184:187], v[118:121]
	v_mfma_f32_16x16x32_bf16 v[114:117], v[174:177], v[184:187], v[114:117]
	v_mfma_f32_16x16x32_bf16 v[102:105], v[166:169], v[192:195], v[102:105]
	v_mfma_f32_16x16x32_bf16 v[98:101], v[174:177], v[192:195], v[98:101]
	v_mfma_f32_16x16x32_bf16 v[82:85], v[166:169], v[200:203], v[82:85]
	v_mfma_f32_16x16x32_bf16 v[74:77], v[174:177], v[200:203], v[74:77]
	v_mfma_f32_16x16x32_bf16 v[70:73], v[166:169], v[208:211], v[70:73]
	v_mfma_f32_16x16x32_bf16 v[66:69], v[174:177], v[208:211], v[66:69]
	v_mfma_f32_16x16x32_bf16 v[118:121], v[170:173], v[188:191], v[118:121]
	v_mfma_f32_16x16x32_bf16 v[114:117], v[178:181], v[188:191], v[114:117]
	v_mfma_f32_16x16x32_bf16 v[102:105], v[170:173], v[196:199], v[102:105]
	v_mfma_f32_16x16x32_bf16 v[98:101], v[178:181], v[196:199], v[98:101]
	v_mfma_f32_16x16x32_bf16 v[82:85], v[170:173], v[204:207], v[82:85]
	v_mfma_f32_16x16x32_bf16 v[74:77], v[178:181], v[204:207], v[74:77]
	v_mfma_f32_16x16x32_bf16 v[70:73], v[170:173], v[212:215], v[70:73]
	v_mfma_f32_16x16x32_bf16 v[66:69], v[178:181], v[212:215], v[66:69]
	s_setprio 0
	s_barrier
	s_nop 0
	s_add_i32 s62, s51, s33
	v_lshl_add_u64 v[216:217], s[34:35], 0, v[130:131]
	s_mov_b32 m0, s62
	ds_read_b128 v[184:187], v153 offset:16384
	ds_read_b128 v[188:191], v153 offset:17408
	ds_read_b128 v[192:195], v153 offset:18432
	ds_read_b128 v[196:199], v153 offset:19456
	ds_read_b128 v[200:203], v153 offset:20480
	ds_read_b128 v[204:207], v153 offset:21504
	ds_read_b128 v[208:211], v153 offset:22528
	ds_read_b128 v[212:215], v153 offset:23552
	global_load_lds_dwordx4 v[216:217], off
	s_add_i32 m0, s62, 0x2000
	s_add_u32 s62, s34, 0x100000
	v_lshl_add_u64 v[218:219], s[34:35], 0, v[132:133]
	s_addc_u32 s63, s35, 0
	s_add_i32 s72, s52, s33
	global_load_lds_dwordx4 v[218:219], off
	v_lshl_add_u64 v[220:221], s[62:63], 0, v[130:131]
	s_mov_b32 m0, s72
	v_lshl_add_u64 v[222:223], s[36:37], 0, v[132:133]
	global_load_lds_dwordx4 v[220:221], off
	v_lshl_add_u64 v[220:221], s[62:63], 0, v[132:133]
	s_add_i32 m0, s72, 0x2000
	s_nop 0
	global_load_lds_dwordx4 v[220:221], off
	v_lshl_add_u64 v[220:221], s[36:37], 0, v[130:131]
	s_mov_b32 m0, s42
	s_nop 0
	global_load_lds_dwordx4 v[220:221], off
	s_mov_b32 m0, s43
	s_nop 0
	global_load_lds_dwordx4 v[222:223], off
	s_waitcnt vmcnt(8)
	s_waitcnt lgkmcnt(0)
	s_barrier
; #define PG8_STAGE(bufoff, gbase, voff) do { _Pragma("unroll") for (int _i = 0; _i < 2; ++_i) \
;         __builtin_amdgcn_global_load_lds((const unsigned*)((const char*)(gbase) + (voff)[_i]), (PG8_LAS unsigned*)(lds + (bufoff) + ldsw + _i * 8192), 16, 0, 0); } while (0)
; #define PG8_LDA(dst, b, h) do { _Pragma("unroll") for (int m = 0; m < 4; ++m) _Pragma("unroll") for (int k = 0; k < 2; ++k) dst[m][k] = *(const PG8_LAS bf16x8*)(lds + PG8_SA(b, h) + aoff + m * 2048 + k * 1024); } while (0)
; #define PG8_LDB(dst, b, h) do { _Pragma("unroll") for (int n = 0; n < 2; ++n) _Pragma("unroll") for (int k = 0; k < 2; ++k) dst[n][k] = *(const PG8_LAS bf16x8*)(lds + PG8_SB(b, h) + boff + n * 2048 + k * 1024); } while (0)
; #define PG8_MMA(ai, bj, At, Bt) do { __builtin_amdgcn_s_setprio(1); _Pragma("unroll") for (int m = 0; m < 4; ++m) _Pragma("unroll") for (int n = 0; n < 2; ++n) _Pragma("unroll") for (int k = 0; k < 2; ++k) \
;         acc[ai][bj][m][n] = __builtin_amdgcn_mfma_f32_16x16x32_bf16(Bt[n][k], At[m][k], acc[ai][bj][m][n], 0, 0, 0); __builtin_amdgcn_s_setprio(0); } while (0)
; #define PG8_WAIT_V(n) asm volatile("s_waitcnt vmcnt(" #n ")" ::: "memory")
; #define PG8_WAIT_L(n) asm volatile("s_waitcnt lgkmcnt(" #n ")" ::: "memory")
; #define PG8_BAR __builtin_amdgcn_s_barrier()
; #define PG8_SCHED __builtin_amdgcn_sched_barrier(0)
; template <class Epi, class Sched, bool ALIGN_EPI = false, bool SP2 = false>
; __device__ __forceinline__ void gemm_phase(PG8_LAS unsigned char* lds, const Gemm g, const Sched& S, const Epi& E) {
;     ...
;             PG8_WAIT_V(8); PG8_WAIT_L(0); PG8_BAR; PG8_MMA(1, 0, At, B0); PG8_MMA(1, 1, At, B1); PG8_BAR; PG8_SCHED;
;             PG8_LDB(B0, 1, 0); PG8_LDB(B1, 1, 1); PG8_SCHED; PG8_LDA(At, 1, 0); PG8_STAGE(PG8_SA(0, 1), a2 + hstep, voffA);
;             PG8_WAIT_V(8); PG8_WAIT_L(0); PG8_BAR; PG8_MMA(0, 0, At, B0); PG8_MMA(0, 1, At, B1); PG8_BAR; PG8_SCHED;
	s_setprio 1
	s_waitcnt lgkmcnt(0)
	v_mfma_f32_16x16x32_bf16 v[62:65], v[142:145], v[184:187], v[62:65]
	v_mfma_f32_16x16x32_bf16 v[58:61], v[158:161], v[184:187], v[58:61]
	v_mfma_f32_16x16x32_bf16 v[50:53], v[142:145], v[192:195], v[50:53]
	v_mfma_f32_16x16x32_bf16 v[42:45], v[158:161], v[192:195], v[42:45]
	v_mfma_f32_16x16x32_bf16 v[34:37], v[142:145], v[200:203], v[34:37]
	v_mfma_f32_16x16x32_bf16 v[26:29], v[158:161], v[200:203], v[26:29]
	v_mfma_f32_16x16x32_bf16 v[14:17], v[142:145], v[208:211], v[14:17]
	v_mfma_f32_16x16x32_bf16 v[10:13], v[158:161], v[208:211], v[10:13]
	v_mfma_f32_16x16x32_bf16 v[62:65], v[154:157], v[188:191], v[62:65]
	v_mfma_f32_16x16x32_bf16 v[58:61], v[162:165], v[188:191], v[58:61]
	v_mfma_f32_16x16x32_bf16 v[50:53], v[154:157], v[196:199], v[50:53]
	v_mfma_f32_16x16x32_bf16 v[42:45], v[162:165], v[196:199], v[42:45]
	v_mfma_f32_16x16x32_bf16 v[34:37], v[154:157], v[204:207], v[34:37]
	v_mfma_f32_16x16x32_bf16 v[26:29], v[162:165], v[204:207], v[26:29]
	v_mfma_f32_16x16x32_bf16 v[14:17], v[154:157], v[212:215], v[14:17]
	v_mfma_f32_16x16x32_bf16 v[10:13], v[162:165], v[212:215], v[10:13]
	s_setprio 0
	s_setprio 1
	v_mfma_f32_16x16x32_bf16 v[54:57], v[166:169], v[184:187], v[54:57]
	v_mfma_f32_16x16x32_bf16 v[46:49], v[174:177], v[184:187], v[46:49]
	v_mfma_f32_16x16x32_bf16 v[38:41], v[166:169], v[192:195], v[38:41]
	v_mfma_f32_16x16x32_bf16 v[30:33], v[174:177], v[192:195], v[30:33]
	v_mfma_f32_16x16x32_bf16 v[22:25], v[166:169], v[200:203], v[22:25]
	v_mfma_f32_16x16x32_bf16 v[18:21], v[174:177], v[200:203], v[18:21]
	v_mfma_f32_16x16x32_bf16 v[6:9], v[166:169], v[208:211], v[6:9]
	v_mfma_f32_16x16x32_bf16 v[2:5], v[174:177], v[208:211], v[2:5]
	v_mfma_f32_16x16x32_bf16 v[54:57], v[170:173], v[188:191], v[54:57]
	v_mfma_f32_16x16x32_bf16 v[46:49], v[178:181], v[188:191], v[46:49]
	v_mfma_f32_16x16x32_bf16 v[38:41], v[170:173], v[196:199], v[38:41]
	v_mfma_f32_16x16x32_bf16 v[30:33], v[178:181], v[196:199], v[30:33]
	v_mfma_f32_16x16x32_bf16 v[22:25], v[170:173], v[204:207], v[22:25]
	v_mfma_f32_16x16x32_bf16 v[18:21], v[178:181], v[204:207], v[18:21]
	v_mfma_f32_16x16x32_bf16 v[6:9], v[170:173], v[212:215], v[6:9]
	v_mfma_f32_16x16x32_bf16 v[2:5], v[178:181], v[212:215], v[2:5]
	s_setprio 0
	s_barrier
	s_nop 0
	s_add_i32 s62, 0, 0x18000
	s_add_i32 s63, 0, 0x1c000
	v_add_u32_e32 v162, s62, v149
	v_add_u32_e32 v178, s63, v149
	ds_read_b128 v[142:145], v162
	ds_read_b128 v[154:157], v162 offset:1024
	ds_read_b128 v[158:161], v162 offset:2048
	ds_read_b128 v[162:165], v162 offset:3072
	ds_read_b128 v[166:169], v178
	ds_read_b128 v[170:173], v178 offset:1024
	ds_read_b128 v[174:177], v178 offset:2048
	ds_read_b128 v[178:181], v178 offset:3072
	s_add_u32 s36, s36, 0x100000
	s_addc_u32 s37, s37, 0
	s_mov_b32 m0, s44
	v_lshl_add_u64 v[224:225], s[36:37], 0, v[130:131]
	ds_read_b128 v[184:187], v153 offset:32768
	ds_read_b128 v[188:191], v153 offset:33792
	ds_read_b128 v[192:195], v153 offset:34816
	ds_read_b128 v[196:199], v153 offset:35840
	ds_read_b128 v[200:203], v153 offset:36864
	ds_read_b128 v[204:207], v153 offset:37888
	ds_read_b128 v[208:211], v153 offset:38912
	ds_read_b128 v[212:215], v153 offset:39936
	global_load_lds_dwordx4 v[224:225], off
	v_lshl_add_u64 v[224:225], s[36:37], 0, v[132:133]
	s_mov_b32 m0, s45
	s_nop 0
	global_load_lds_dwordx4 v[224:225], off
	s_waitcnt vmcnt(8)
	s_waitcnt lgkmcnt(0)
	s_barrier
	s_setprio 1
	s_waitcnt lgkmcnt(0)
	v_mfma_f32_16x16x32_bf16 v[126:129], v[142:145], v[184:187], v[126:129]
	v_mfma_f32_16x16x32_bf16 v[122:125], v[158:161], v[184:187], v[122:125]
	v_mfma_f32_16x16x32_bf16 v[110:113], v[142:145], v[192:195], v[110:113]
	v_mfma_f32_16x16x32_bf16 v[106:109], v[158:161], v[192:195], v[106:109]
	v_mfma_f32_16x16x32_bf16 v[94:97], v[142:145], v[200:203], v[94:97]
	v_mfma_f32_16x16x32_bf16 v[90:93], v[158:161], v[200:203], v[90:93]
	v_mfma_f32_16x16x32_bf16 v[86:89], v[142:145], v[208:211], v[86:89]
	v_mfma_f32_16x16x32_bf16 v[78:81], v[158:161], v[208:211], v[78:81]
	v_mfma_f32_16x16x32_bf16 v[126:129], v[154:157], v[188:191], v[126:129]
	v_mfma_f32_16x16x32_bf16 v[122:125], v[162:165], v[188:191], v[122:125]
	v_mfma_f32_16x16x32_bf16 v[110:113], v[154:157], v[196:199], v[110:113]
	v_mfma_f32_16x16x32_bf16 v[106:109], v[162:165], v[196:199], v[106:109]
	v_mfma_f32_16x16x32_bf16 v[94:97], v[154:157], v[204:207], v[94:97]
	v_mfma_f32_16x16x32_bf16 v[90:93], v[162:165], v[204:207], v[90:93]
	v_mfma_f32_16x16x32_bf16 v[86:89], v[154:157], v[212:215], v[86:89]
	v_mfma_f32_16x16x32_bf16 v[78:81], v[162:165], v[212:215], v[78:81]
	s_setprio 0
	s_setprio 1
	v_mfma_f32_16x16x32_bf16 v[118:121], v[166:169], v[184:187], v[118:121]
	v_mfma_f32_16x16x32_bf16 v[114:117], v[174:177], v[184:187], v[114:117]
	v_mfma_f32_16x16x32_bf16 v[102:105], v[166:169], v[192:195], v[102:105]
	v_mfma_f32_16x16x32_bf16 v[98:101], v[174:177], v[192:195], v[98:101]
	v_mfma_f32_16x16x32_bf16 v[82:85], v[166:169], v[200:203], v[82:85]
	v_mfma_f32_16x16x32_bf16 v[74:77], v[174:177], v[200:203], v[74:77]
	v_mfma_f32_16x16x32_bf16 v[70:73], v[166:169], v[208:211], v[70:73]
	v_mfma_f32_16x16x32_bf16 v[66:69], v[174:177], v[208:211], v[66:69]
	v_mfma_f32_16x16x32_bf16 v[118:121], v[170:173], v[188:191], v[118:121]
	v_mfma_f32_16x16x32_bf16 v[114:117], v[178:181], v[188:191], v[114:117]
	v_mfma_f32_16x16x32_bf16 v[102:105], v[170:173], v[196:199], v[102:105]
	v_mfma_f32_16x16x32_bf16 v[98:101], v[178:181], v[196:199], v[98:101]
	v_mfma_f32_16x16x32_bf16 v[82:85], v[170:173], v[204:207], v[82:85]
	v_mfma_f32_16x16x32_bf16 v[74:77], v[178:181], v[204:207], v[74:77]
	v_mfma_f32_16x16x32_bf16 v[70:73], v[170:173], v[212:215], v[70:73]
	v_mfma_f32_16x16x32_bf16 v[66:69], v[178:181], v[212:215], v[66:69]
	s_setprio 0
	s_barrier
; #define PG8_STAGE(bufoff, gbase, voff) do { _Pragma("unroll") for (int _i = 0; _i < 2; ++_i) \
;         __builtin_amdgcn_global_load_lds((const unsigned*)((const char*)(gbase) + (voff)[_i]), (PG8_LAS unsigned*)(lds + (bufoff) + ldsw + _i * 8192), 16, 0, 0); } while (0)
; #define PG8_LDA(dst, b, h) do { _Pragma("unroll") for (int m = 0; m < 4; ++m) _Pragma("unroll") for (int k = 0; k < 2; ++k) dst[m][k] = *(const PG8_LAS bf16x8*)(lds + PG8_SA(b, h) + aoff + m * 2048 + k * 1024); } while (0)
; #define PG8_MMA(ai, bj, At, Bt) do { __builtin_amdgcn_s_setprio(1); _Pragma("unroll") for (int m = 0; m < 4; ++m) _Pragma("unroll") for (int n = 0; n < 2; ++n) _Pragma("unroll") for (int k = 0; k < 2; ++k) \
;         acc[ai][bj][m][n] = __builtin_amdgcn_mfma_f32_16x16x32_bf16(Bt[n][k], At[m][k], acc[ai][bj][m][n], 0, 0, 0); __builtin_amdgcn_s_setprio(0); } while (0)
; #define PG8_WAIT_V(n) asm volatile("s_waitcnt vmcnt(" #n ")" ::: "memory")
; #define PG8_WAIT_L(n) asm volatile("s_waitcnt lgkmcnt(" #n ")" ::: "memory")
; #define PG8_BAR __builtin_amdgcn_s_barrier()
; #define PG8_SCHED __builtin_amdgcn_sched_barrier(0)
; template <class Epi, class Sched, bool ALIGN_EPI = false, bool SP2 = false>
; __device__ __forceinline__ void gemm_phase(PG8_LAS unsigned char* lds, const Gemm g, const Sched& S, const Epi& E) {
;     ...
;         for (int t = 0; t < nt; t += 2) {
;     ...
;             PG8_LDA(At, 1, 1); PG8_STAGE(PG8_SB(1, 0), b3, voffB); PG8_STAGE(PG8_SB(1, 1), b3 + hstep, voffB); PG8_STAGE(PG8_SA(1, 0), a3, voffA);
;             PG8_WAIT_V(8); PG8_WAIT_L(0); PG8_BAR; PG8_MMA(1, 0, At, B0); PG8_MMA(1, 1, At, B1); PG8_BAR; PG8_SCHED;
	s_add_i32 s36, s62, s33
	v_lshl_add_u64 v[216:217], v[216:217], 0, s[12:13]
	s_mov_b32 m0, s36
	ds_read_b128 v[184:187], v153 offset:49152
	ds_read_b128 v[188:191], v153 offset:50176
	ds_read_b128 v[192:195], v153 offset:51200
	ds_read_b128 v[196:199], v153 offset:52224
	ds_read_b128 v[200:203], v153 offset:53248
	ds_read_b128 v[204:207], v153 offset:54272
	ds_read_b128 v[208:211], v153 offset:55296
	ds_read_b128 v[212:215], v153 offset:56320
	global_load_lds_dwordx4 v[216:217], off
	s_add_i32 m0, s36, 0x2000
	s_add_u32 s34, s34, 0x100080
	v_lshl_add_u64 v[216:217], v[218:219], 0, s[12:13]
	s_addc_u32 s35, s35, 0
	s_add_i32 s36, s63, s33
	global_load_lds_dwordx4 v[216:217], off
	v_lshl_add_u64 v[216:217], s[34:35], 0, v[130:131]
	s_mov_b32 m0, s36
	s_nop 0
	global_load_lds_dwordx4 v[216:217], off
	v_lshl_add_u64 v[216:217], s[34:35], 0, v[132:133]
	s_add_i32 m0, s36, 0x2000
	s_nop 0
	global_load_lds_dwordx4 v[216:217], off
	v_lshl_add_u64 v[216:217], v[220:221], 0, s[12:13]
	s_mov_b32 m0, s49
	s_nop 0
	global_load_lds_dwordx4 v[216:217], off
	v_lshl_add_u64 v[216:217], v[222:223], 0, s[12:13]
	s_mov_b32 m0, s50
	s_nop 0
	global_load_lds_dwordx4 v[216:217], off
	s_waitcnt vmcnt(8)
	s_waitcnt lgkmcnt(0)
	s_barrier
	s_setprio 1
	s_waitcnt lgkmcnt(0)
	v_mfma_f32_16x16x32_bf16 v[62:65], v[142:145], v[184:187], v[62:65]
	v_mfma_f32_16x16x32_bf16 v[58:61], v[158:161], v[184:187], v[58:61]
	v_mfma_f32_16x16x32_bf16 v[50:53], v[142:145], v[192:195], v[50:53]
	v_mfma_f32_16x16x32_bf16 v[42:45], v[158:161], v[192:195], v[42:45]
	v_mfma_f32_16x16x32_bf16 v[34:37], v[142:145], v[200:203], v[34:37]
	v_mfma_f32_16x16x32_bf16 v[26:29], v[158:161], v[200:203], v[26:29]
	v_mfma_f32_16x16x32_bf16 v[14:17], v[142:145], v[208:211], v[14:17]
	v_mfma_f32_16x16x32_bf16 v[10:13], v[158:161], v[208:211], v[10:13]
	v_mfma_f32_16x16x32_bf16 v[62:65], v[154:157], v[188:191], v[62:65]
	v_mfma_f32_16x16x32_bf16 v[58:61], v[162:165], v[188:191], v[58:61]
	v_mfma_f32_16x16x32_bf16 v[50:53], v[154:157], v[196:199], v[50:53]
	v_mfma_f32_16x16x32_bf16 v[42:45], v[162:165], v[196:199], v[42:45]
	v_mfma_f32_16x16x32_bf16 v[34:37], v[154:157], v[204:207], v[34:37]
	v_mfma_f32_16x16x32_bf16 v[26:29], v[162:165], v[204:207], v[26:29]
	v_mfma_f32_16x16x32_bf16 v[14:17], v[154:157], v[212:215], v[14:17]
	v_mfma_f32_16x16x32_bf16 v[10:13], v[162:165], v[212:215], v[10:13]
	s_setprio 0
	s_setprio 1
	v_mfma_f32_16x16x32_bf16 v[54:57], v[166:169], v[184:187], v[54:57]
	v_mfma_f32_16x16x32_bf16 v[46:49], v[174:177], v[184:187], v[46:49]
	v_mfma_f32_16x16x32_bf16 v[38:41], v[166:169], v[192:195], v[38:41]
	v_mfma_f32_16x16x32_bf16 v[30:33], v[174:177], v[192:195], v[30:33]
	v_mfma_f32_16x16x32_bf16 v[22:25], v[166:169], v[200:203], v[22:25]
	v_mfma_f32_16x16x32_bf16 v[18:21], v[174:177], v[200:203], v[18:21]
	v_mfma_f32_16x16x32_bf16 v[6:9], v[166:169], v[208:211], v[6:9]
	v_mfma_f32_16x16x32_bf16 v[2:5], v[174:177], v[208:211], v[2:5]
	v_mfma_f32_16x16x32_bf16 v[54:57], v[170:173], v[188:191], v[54:57]
	v_mfma_f32_16x16x32_bf16 v[46:49], v[178:181], v[188:191], v[46:49]
	v_mfma_f32_16x16x32_bf16 v[38:41], v[170:173], v[196:199], v[38:41]
	v_mfma_f32_16x16x32_bf16 v[30:33], v[178:181], v[196:199], v[30:33]
	v_mfma_f32_16x16x32_bf16 v[22:25], v[170:173], v[204:207], v[22:25]
	v_mfma_f32_16x16x32_bf16 v[18:21], v[178:181], v[204:207], v[18:21]
	v_mfma_f32_16x16x32_bf16 v[6:9], v[170:173], v[212:215], v[6:9]
	v_mfma_f32_16x16x32_bf16 v[2:5], v[178:181], v[212:215], v[2:5]
	s_setprio 0
	s_barrier
	s_add_i32 s61, s61, 2
	s_add_u32 s30, s30, 0x100
	s_addc_u32 s31, s31, 0
	s_add_u32 s59, s59, 0x100
	s_addc_u32 s60, s60, 0
	s_cmp_gt_u32 s61, 61
	s_cbranch_scc0 .LBB0_707
	s_and_b64 vcc, exec, s[14:15]
	s_cbranch_vccz .LBB0_710
	s_barrier
